# hand-written proj-GEMM epilogue (P3): same products, no dead rstd reduction code
# baseline (speedup 1.0000x reference)
; __device__ __forceinline__ unsigned cvt_pk_bf16(float lo, float hi) { unsigned r; asm volatile("v_cvt_pk_bf16_f32 %0, %1, %2" : "=v"(r) : "v"(lo), "v"(hi)); return r; }
; __device__ __forceinline__ int fresh_lane() { int l; asm volatile("v_mbcnt_lo_u32_b32 %0, -1, 0\n\tv_mbcnt_hi_u32_b32 %0, -1, %0" : "=v"(l)); return l; }
; __device__ __forceinline__ void store16_wt(__amdgpu_buffer_rsrc_t rsrc, unsigned byte_off, v4u v) { __builtin_amdgcn_raw_buffer_store_b128(v, rsrc, byte_off, 0, 16); }
;     __device__ __forceinline__ void operator()(AccRef acc, const Unit& u, int wr, int wc, int, int) const {
;         const int ln_ = fresh_lane(), fr = ln_ & 15, fq = ln_ >> 4;
;         const int row0 = u.pm * 256 + wr * 64 + fr, col0 = u.pn * 256 + wc * 32 + 8 * fq;
;         const __amdgpu_buffer_rsrc_t rsrc = __builtin_amdgcn_make_buffer_rsrc((void*)O, 0, (int)((size_t)M * DINP * 2), 0x00020000);
;         float rs[8]; rows_rstd(ss, row0, fq, ln_, rs);
; #pragma unroll
;         for (int ai = 0; ai < 2; ++ai)
; #pragma unroll
;             for (int m = 0; m < 4; ++m) {
;                 const int row = row0 + ai * 128 + m * 16;
;                 const float r = rs[ai * 4 + m];
; #pragma unroll
;                 for (int bj = 0; bj < 2; ++bj) {
;                     const f32x4 v0 = acc[ai][bj][m][0] * r, v1 = acc[ai][bj][m][1] * r;
;                     v4u w; w.x = cvt_pk_bf16(v0[0], v0[1]); w.y = cvt_pk_bf16(v0[2], v0[3]); w.z = cvt_pk_bf16(v1[0], v1[1]); w.w = cvt_pk_bf16(v1[2], v1[3]);
;                     store16_wt(rsrc, (unsigned)(((size_t)row * DINP + col0 + bj * 128) * 2), w);
;                 }
;             }
;     }
.LBB0_342:
	s_lshl_b32 s98, s6, 8
	v_mbcnt_lo_u32_b32 v130, -1, 0
	v_mbcnt_hi_u32_b32 v130, -1, v130
	s_add_i32 s98, s98, s38
	s_lshl_b32 s99, s7, 8
	s_or_b32 s99, s99, s39
	v_and_or_b32 v131, v130, 15, s98
	v_lshrrev_b32_e32 v132, 4, v130
	v_lshl_add_u32 v132, v132, 3, s99
	s_movk_i32 s98, 0x3c00
	v_mul_lo_u32 v131, v131, s98
	v_readlane_b32 s20, v254, 19
	v_readlane_b32 s21, v254, 20
	v_readlane_b32 s22, v254, 21
	v_readlane_b32 s23, v254, 22
	v_add_lshl_u32 v131, v132, v131, 1
	v_mov_b32_e32 v133, v131
	v_mul_f32_e32 v126, v242, v126
	v_mul_f32_e32 v127, v242, v127
	v_mul_f32_e32 v128, v242, v128
	v_mul_f32_e32 v129, v242, v129
	v_mul_f32_e32 v122, v242, v122
	v_mul_f32_e32 v123, v242, v123
	v_mul_f32_e32 v124, v242, v124
	v_mul_f32_e32 v125, v242, v125
	v_cvt_pk_bf16_f32 v148, v126, v127
	v_cvt_pk_bf16_f32 v149, v128, v129
	v_cvt_pk_bf16_f32 v150, v122, v123
	v_cvt_pk_bf16_f32 v151, v124, v125
	buffer_store_dwordx4 v[148:151], v133, s[20:23], 0 offen sc1
	v_mul_f32_e32 v118, v242, v118
	v_mul_f32_e32 v119, v242, v119
	v_mul_f32_e32 v120, v242, v120
	v_mul_f32_e32 v121, v242, v121
	v_mul_f32_e32 v110, v242, v110
	v_mul_f32_e32 v111, v242, v111
	v_mul_f32_e32 v112, v242, v112
	v_mul_f32_e32 v113, v242, v113
	v_cvt_pk_bf16_f32 v152, v118, v119
	v_cvt_pk_bf16_f32 v153, v120, v121
	v_cvt_pk_bf16_f32 v154, v110, v111
	v_cvt_pk_bf16_f32 v155, v112, v113
	buffer_store_dwordx4 v[152:155], v133, s[20:23], 0 offen offset:256 sc1
	v_add_u32_e32 v133, 0x78000, v131
	v_mul_f32_e32 v114, v243, v114
	v_mul_f32_e32 v115, v243, v115
	v_mul_f32_e32 v116, v243, v116
	v_mul_f32_e32 v117, v243, v117
	v_mul_f32_e32 v106, v243, v106
	v_mul_f32_e32 v107, v243, v107
	v_mul_f32_e32 v108, v243, v108
	v_mul_f32_e32 v109, v243, v109
	v_cvt_pk_bf16_f32 v156, v114, v115
	v_cvt_pk_bf16_f32 v157, v116, v117
	v_cvt_pk_bf16_f32 v158, v106, v107
	v_cvt_pk_bf16_f32 v159, v108, v109
	buffer_store_dwordx4 v[156:159], v133, s[20:23], 0 offen sc1
	v_mul_f32_e32 v102, v243, v102
	v_mul_f32_e32 v103, v243, v103
	v_mul_f32_e32 v104, v243, v104
	v_mul_f32_e32 v105, v243, v105
	v_mul_f32_e32 v94, v243, v94
	v_mul_f32_e32 v95, v243, v95
	v_mul_f32_e32 v96, v243, v96
	v_mul_f32_e32 v97, v243, v97
	v_cvt_pk_bf16_f32 v160, v102, v103
	v_cvt_pk_bf16_f32 v161, v104, v105
	v_cvt_pk_bf16_f32 v162, v94, v95
	v_cvt_pk_bf16_f32 v163, v96, v97
	buffer_store_dwordx4 v[160:163], v133, s[20:23], 0 offen offset:256 sc1
	v_add_u32_e32 v133, 0xf0000, v131
	v_mul_f32_e32 v98, v244, v98
	v_mul_f32_e32 v99, v244, v99
	v_mul_f32_e32 v100, v244, v100
	v_mul_f32_e32 v101, v244, v101
	v_mul_f32_e32 v90, v244, v90
	v_mul_f32_e32 v91, v244, v91
	v_mul_f32_e32 v92, v244, v92
	v_mul_f32_e32 v93, v244, v93
	v_cvt_pk_bf16_f32 v148, v98, v99
	v_cvt_pk_bf16_f32 v149, v100, v101
	v_cvt_pk_bf16_f32 v150, v90, v91
	v_cvt_pk_bf16_f32 v151, v92, v93
	buffer_store_dwordx4 v[148:151], v133, s[20:23], 0 offen sc1
	v_mul_f32_e32 v86, v244, v86
	v_mul_f32_e32 v87, v244, v87
	v_mul_f32_e32 v88, v244, v88
	v_mul_f32_e32 v89, v244, v89
	v_mul_f32_e32 v78, v244, v78
	v_mul_f32_e32 v79, v244, v79
	v_mul_f32_e32 v80, v244, v80
	v_mul_f32_e32 v81, v244, v81
	v_cvt_pk_bf16_f32 v152, v86, v87
	v_cvt_pk_bf16_f32 v153, v88, v89
	v_cvt_pk_bf16_f32 v154, v78, v79
	v_cvt_pk_bf16_f32 v155, v80, v81
	buffer_store_dwordx4 v[152:155], v133, s[20:23], 0 offen offset:256 sc1
	v_add_u32_e32 v133, 0x168000, v131
	v_mul_f32_e32 v82, v245, v82
	v_mul_f32_e32 v83, v245, v83
	v_mul_f32_e32 v84, v245, v84
	v_mul_f32_e32 v85, v245, v85
	v_mul_f32_e32 v74, v245, v74
	v_mul_f32_e32 v75, v245, v75
	v_mul_f32_e32 v76, v245, v76
	v_mul_f32_e32 v77, v245, v77
	v_cvt_pk_bf16_f32 v156, v82, v83
	v_cvt_pk_bf16_f32 v157, v84, v85
	v_cvt_pk_bf16_f32 v158, v74, v75
	v_cvt_pk_bf16_f32 v159, v76, v77
	buffer_store_dwordx4 v[156:159], v133, s[20:23], 0 offen sc1
	v_mul_f32_e32 v70, v245, v70
	v_mul_f32_e32 v71, v245, v71
	v_mul_f32_e32 v72, v245, v72
	v_mul_f32_e32 v73, v245, v73
	v_mul_f32_e32 v66, v245, v66
	v_mul_f32_e32 v67, v245, v67
	v_mul_f32_e32 v68, v245, v68
	v_mul_f32_e32 v69, v245, v69
; __device__ __forceinline__ unsigned cvt_pk_bf16(float lo, float hi) { unsigned r; asm volatile("v_cvt_pk_bf16_f32 %0, %1, %2" : "=v"(r) : "v"(lo), "v"(hi)); return r; }
; #define PG8_BAR __builtin_amdgcn_s_barrier()
; __device__ __forceinline__ void store16_wt(__amdgpu_buffer_rsrc_t rsrc, unsigned byte_off, v4u v) { __builtin_amdgcn_raw_buffer_store_b128(v, rsrc, byte_off, 0, 16); }
; template <class Epi, class Sched, bool ALIGN_EPI = false, bool SP2 = false>
; __device__ __forceinline__ void gemm_phase(PG8_LAS unsigned char* lds, const Gemm g, const Sched& S, const Epi& E, int tid_) {
;     ...
;         if constexpr (ALIGN_EPI) { if (wr == 0) PG8_BAR; }
;         E(acc, cur, wr, wc, fr, fq); S.done(cur);
;         if (!has_next) break;
;         if (!(Epi::KEEP && E.keep(cur))) {
; #pragma unroll
;         for (int a = 0; a < 2; ++a)
; #pragma unroll
;             for (int b = 0; b < 2; ++b)
; #pragma unroll
;                 for (int m = 0; m < 4; ++m)
; #pragma unroll
;                     for (int n = 0; n < 2; ++n) acc[a][b][m][n] = (f32x4){0.f, 0.f, 0.f, 0.f};
;         }
;         cur = nxt; cA = nA; cB = nB; ++ui;
;         if constexpr (ALIGN_EPI) { if (wr == 1) PG8_BAR; }
;     __device__ __forceinline__ void operator()(AccRef acc, const Unit& u, int wr, int wc, int, int) const {
;     ...
; #pragma unroll
;                 for (int bj = 0; bj < 2; ++bj) {
;                     const f32x4 v0 = acc[ai][bj][m][0] * r, v1 = acc[ai][bj][m][1] * r;
;                     v4u w; w.x = cvt_pk_bf16(v0[0], v0[1]); w.y = cvt_pk_bf16(v0[2], v0[3]); w.z = cvt_pk_bf16(v1[0], v1[1]); w.w = cvt_pk_bf16(v1[2], v1[3]);
;                     store16_wt(rsrc, (unsigned)(((size_t)row * DINP + col0 + bj * 128) * 2), w);
;                 }
	v_cvt_pk_bf16_f32 v160, v70, v71
	v_cvt_pk_bf16_f32 v161, v72, v73
	v_cvt_pk_bf16_f32 v162, v66, v67
	v_cvt_pk_bf16_f32 v163, v68, v69
	buffer_store_dwordx4 v[160:163], v133, s[20:23], 0 offen offset:256 sc1
	v_add_u32_e32 v133, 0x3c0000, v131
	v_mul_f32_e32 v62, v246, v62
	v_mul_f32_e32 v63, v246, v63
	v_mul_f32_e32 v64, v246, v64
	v_mul_f32_e32 v65, v246, v65
	v_mul_f32_e32 v58, v246, v58
	v_mul_f32_e32 v59, v246, v59
	v_mul_f32_e32 v60, v246, v60
	v_mul_f32_e32 v61, v246, v61
	v_cvt_pk_bf16_f32 v148, v62, v63
	v_cvt_pk_bf16_f32 v149, v64, v65
	v_cvt_pk_bf16_f32 v150, v58, v59
	v_cvt_pk_bf16_f32 v151, v60, v61
	buffer_store_dwordx4 v[148:151], v133, s[20:23], 0 offen sc1
	v_mul_f32_e32 v54, v246, v54
	v_mul_f32_e32 v55, v246, v55
	v_mul_f32_e32 v56, v246, v56
	v_mul_f32_e32 v57, v246, v57
	v_mul_f32_e32 v46, v246, v46
	v_mul_f32_e32 v47, v246, v47
	v_mul_f32_e32 v48, v246, v48
	v_mul_f32_e32 v49, v246, v49
	v_cvt_pk_bf16_f32 v152, v54, v55
	v_cvt_pk_bf16_f32 v153, v56, v57
	v_cvt_pk_bf16_f32 v154, v46, v47
	v_cvt_pk_bf16_f32 v155, v48, v49
	buffer_store_dwordx4 v[152:155], v133, s[20:23], 0 offen offset:256 sc1
	v_add_u32_e32 v133, 0x438000, v131
	v_mul_f32_e32 v50, v247, v50
	v_mul_f32_e32 v51, v247, v51
	v_mul_f32_e32 v52, v247, v52
	v_mul_f32_e32 v53, v247, v53
	v_mul_f32_e32 v42, v247, v42
	v_mul_f32_e32 v43, v247, v43
	v_mul_f32_e32 v44, v247, v44
	v_mul_f32_e32 v45, v247, v45
	v_cvt_pk_bf16_f32 v156, v50, v51
	v_cvt_pk_bf16_f32 v157, v52, v53
	v_cvt_pk_bf16_f32 v158, v42, v43
	v_cvt_pk_bf16_f32 v159, v44, v45
	buffer_store_dwordx4 v[156:159], v133, s[20:23], 0 offen sc1
	v_mul_f32_e32 v38, v247, v38
	v_mul_f32_e32 v39, v247, v39
	v_mul_f32_e32 v40, v247, v40
	v_mul_f32_e32 v41, v247, v41
	v_mul_f32_e32 v30, v247, v30
	v_mul_f32_e32 v31, v247, v31
	v_mul_f32_e32 v32, v247, v32
	v_mul_f32_e32 v33, v247, v33
	v_cvt_pk_bf16_f32 v160, v38, v39
	v_cvt_pk_bf16_f32 v161, v40, v41
	v_cvt_pk_bf16_f32 v162, v30, v31
	v_cvt_pk_bf16_f32 v163, v32, v33
	buffer_store_dwordx4 v[160:163], v133, s[20:23], 0 offen offset:256 sc1
	v_add_u32_e32 v133, 0x4b0000, v131
	v_mul_f32_e32 v34, v248, v34
	v_mul_f32_e32 v35, v248, v35
	v_mul_f32_e32 v36, v248, v36
	v_mul_f32_e32 v37, v248, v37
	v_mul_f32_e32 v26, v248, v26
	v_mul_f32_e32 v27, v248, v27
	v_mul_f32_e32 v28, v248, v28
	v_mul_f32_e32 v29, v248, v29
	v_cvt_pk_bf16_f32 v148, v34, v35
	v_cvt_pk_bf16_f32 v149, v36, v37
	v_cvt_pk_bf16_f32 v150, v26, v27
	v_cvt_pk_bf16_f32 v151, v28, v29
	buffer_store_dwordx4 v[148:151], v133, s[20:23], 0 offen sc1
	v_mul_f32_e32 v22, v248, v22
	v_mul_f32_e32 v23, v248, v23
	v_mul_f32_e32 v24, v248, v24
	v_mul_f32_e32 v25, v248, v25
	v_mul_f32_e32 v14, v248, v14
	v_mul_f32_e32 v15, v248, v15
	v_mul_f32_e32 v16, v248, v16
	v_mul_f32_e32 v17, v248, v17
	v_cvt_pk_bf16_f32 v152, v22, v23
	v_cvt_pk_bf16_f32 v153, v24, v25
	v_cvt_pk_bf16_f32 v154, v14, v15
	v_cvt_pk_bf16_f32 v155, v16, v17
	buffer_store_dwordx4 v[152:155], v133, s[20:23], 0 offen offset:256 sc1
	v_add_u32_e32 v133, 0x528000, v131
	v_mul_f32_e32 v18, v249, v18
	v_mul_f32_e32 v19, v249, v19
	v_mul_f32_e32 v20, v249, v20
	v_mul_f32_e32 v21, v249, v21
	v_mul_f32_e32 v10, v249, v10
	v_mul_f32_e32 v11, v249, v11
	v_mul_f32_e32 v12, v249, v12
	v_mul_f32_e32 v13, v249, v13
	v_cvt_pk_bf16_f32 v156, v18, v19
	v_cvt_pk_bf16_f32 v157, v20, v21
	v_cvt_pk_bf16_f32 v158, v10, v11
	v_cvt_pk_bf16_f32 v159, v12, v13
	buffer_store_dwordx4 v[156:159], v133, s[20:23], 0 offen sc1
	v_mul_f32_e32 v4, v249, v4
	v_mul_f32_e32 v5, v249, v5
	v_mul_f32_e32 v6, v249, v6
	v_mul_f32_e32 v7, v249, v7
	v_mul_f32_e32 v0, v249, v0
	v_mul_f32_e32 v1, v249, v1
	v_mul_f32_e32 v2, v249, v2
	v_mul_f32_e32 v3, v249, v3
	v_cvt_pk_bf16_f32 v160, v4, v5
	v_cvt_pk_bf16_f32 v161, v6, v7
	v_cvt_pk_bf16_f32 v162, v0, v1
	v_cvt_pk_bf16_f32 v163, v2, v3
	buffer_store_dwordx4 v[160:163], v133, s[20:23], 0 offen offset:256 sc1
	s_mov_b64 s[6:7], -1
	s_andn2_b64 vcc, exec, s[4:5]
	s_cbranch_vccnz .LBB0_335
	s_andn2_b64 vcc, exec, s[0:1]
	s_cbranch_vccnz .LBB0_334
	s_barrier
	s_branch .LBB0_334
